# phase M: de-serialised conditional-load ladders (8 rstd loads in epilogue, 4 token-id loads at unit boundary: all in flight then one wait) + in-proj weight prefetch
# speedup vs baseline: 1.0173x; 1.0018x over previous
.LBB0_5221:
	v_add_u32_e32 v2, 0, v250
	v_add_u32_e32 v3, 0x10000, v2
	v_add_u32_e32 v14, 0x14000, v2
	ds_read_b128 v[18:21], v3
	ds_read_b128 v[22:25], v3 offset:1024
	ds_read_b128 v[26:29], v3 offset:2048
	ds_read_b128 v[30:33], v3 offset:3072
	ds_read_b128 v[2:5], v14
	ds_read_b128 v[6:9], v14 offset:1024
	ds_read_b128 v[10:13], v14 offset:2048
	ds_read_b128 v[14:17], v14 offset:3072
	s_cmp_eq_u32 s71, 12
	s_cselect_b64 s[36:37], -1, 0
	s_add_i32 m0, s31, 0xc000
	ds_read_b128 v[58:61], v251
	ds_read_b128 v[62:65], v251 offset:1024
	ds_read_b128 v[50:53], v251 offset:2048
	ds_read_b128 v[54:57], v251 offset:3072
	ds_read_b128 v[42:45], v251 offset:4096
	ds_read_b128 v[46:49], v251 offset:5120
	ds_read_b128 v[34:37], v251 offset:6144
	ds_read_b128 v[38:41], v251 offset:7168
	global_load_lds_dwordx4 v0, s[34:35]
	s_add_i32 m0, s31, 0xe000
	s_and_b64 s[38:39], s[26:27], s[36:37]
	global_load_lds_dwordx4 v206, s[34:35]
	s_andn2_b64 vcc, exec, s[38:39]
	s_cbranch_vccnz .LBB0_5220
	v_mov_b32_e32 v0, s67
	ds_read_b32 v202, v0 offset:68
	v_mov_b32_e32 v203, 0
	v_mov_b32_e32 v205, 0
	s_waitcnt lgkmcnt(0)
	v_readfirstlane_b32 s0, v202
	v_mov_b32_e32 v0, 0
	v_mov_b32_e32 v202, 0
	s_nop 1
	v_cmp_gt_i32_e32 vcc, s0, v252
	s_and_saveexec_b64 s[38:39], vcc
	s_nop 0
	global_load_dword v203, v[208:209], off
	s_mov_b64 exec, s[38:39]
	v_cmp_gt_i32_e32 vcc, s0, v253
	s_and_saveexec_b64 s[38:39], vcc
	s_nop 0
	global_load_dword v0, v[210:211], off
	s_mov_b64 exec, s[38:39]
	v_cmp_gt_i32_e32 vcc, s0, v236
	s_and_saveexec_b64 s[38:39], vcc
	s_nop 0
	global_load_dword v202, v[212:213], off
	s_mov_b64 exec, s[38:39]
	v_cmp_gt_i32_e32 vcc, s0, v223
	s_and_saveexec_b64 s[38:39], vcc
	s_nop 0
	global_load_dword v205, v[214:215], off
	s_mov_b64 exec, s[38:39]
	s_waitcnt vmcnt(0)
	v_lshlrev_b32_e32 v203, 11, v203
	v_lshlrev_b32_e32 v0, 11, v0
	v_lshlrev_b32_e32 v202, 11, v202
	v_lshlrev_b32_e32 v205, 11, v205
	s_branch .LBB0_5219

.LBB0_5232:
	s_lshl_b32 s0, s64, 2
	s_add_i32 s0, s0, 0
	s_add_i32 s0, s0, 0x20244
	v_mov_b32_e32 v2, v249
	v_mov_b32_e32 v3, v248
	v_mov_b32_e32 v4, s0
	ds_read_b32 v4, v4
	v_add_u32_e32 v5, s54, v3
	v_lshl_add_u32 v3, s65, 8, v5
	s_lshl_b32 s0, s64, 14
	v_mov_b32_e32 v18, 0
	s_waitcnt lgkmcnt(0)
	v_readfirstlane_b32 s25, v4
	v_mov_b32_e32 v20, 0
	s_nop 0
	v_readlane_b32 s66, v254, 46
	v_readlane_b32 s67, v254, 47
	v_readlane_b32 s71, v254, 49
	v_mov_b32_e32 v20, 0
	v_mov_b32_e32 v18, 0
	v_mov_b32_e32 v16, 0
	v_mov_b32_e32 v14, 0
	v_mov_b32_e32 v12, 0
	v_mov_b32_e32 v10, 0
	v_mov_b32_e32 v8, 0
	v_mov_b32_e32 v4, 0
	v_mov_b32_e32 v6, v3
	v_cmp_gt_i32_e32 vcc, s25, v6
	s_and_saveexec_b64 s[34:35], vcc
	v_add_u32_e32 v6, s0, v6
	v_ashrrev_i32_e32 v7, 31, v6
	v_lshl_add_u64 v[6:7], v[6:7], 2, s[18:19]
	global_load_dword v20, v[6:7], off
	s_mov_b64 exec, s[34:35]
	v_add_u32_e32 v6, 0x10, v3
	v_cmp_gt_i32_e32 vcc, s25, v6
	s_and_saveexec_b64 s[34:35], vcc
	v_add_u32_e32 v6, s0, v6
	v_ashrrev_i32_e32 v7, 31, v6
	v_lshl_add_u64 v[6:7], v[6:7], 2, s[18:19]
	global_load_dword v18, v[6:7], off
	s_mov_b64 exec, s[34:35]
	v_add_u32_e32 v6, 0x20, v3
	v_cmp_gt_i32_e32 vcc, s25, v6
	s_and_saveexec_b64 s[34:35], vcc
	v_add_u32_e32 v6, s0, v6
	v_ashrrev_i32_e32 v7, 31, v6
	v_lshl_add_u64 v[6:7], v[6:7], 2, s[18:19]
	global_load_dword v16, v[6:7], off
	s_mov_b64 exec, s[34:35]
	v_add_u32_e32 v6, 0x30, v3
	v_cmp_gt_i32_e32 vcc, s25, v6
	s_and_saveexec_b64 s[34:35], vcc
	v_add_u32_e32 v6, s0, v6
	v_ashrrev_i32_e32 v7, 31, v6
	v_lshl_add_u64 v[6:7], v[6:7], 2, s[18:19]
	global_load_dword v14, v[6:7], off
	s_mov_b64 exec, s[34:35]
	v_add_u32_e32 v6, 0x80, v3
	v_cmp_gt_i32_e32 vcc, s25, v6
	s_and_saveexec_b64 s[34:35], vcc
	v_add_u32_e32 v6, s0, v6
	v_ashrrev_i32_e32 v7, 31, v6
	v_lshl_add_u64 v[6:7], v[6:7], 2, s[18:19]
	global_load_dword v12, v[6:7], off
	s_mov_b64 exec, s[34:35]
	v_add_u32_e32 v6, 0x90, v3
	v_cmp_gt_i32_e32 vcc, s25, v6
	s_and_saveexec_b64 s[34:35], vcc
	v_add_u32_e32 v6, s0, v6
	v_ashrrev_i32_e32 v7, 31, v6
	v_lshl_add_u64 v[6:7], v[6:7], 2, s[18:19]
	global_load_dword v10, v[6:7], off
	s_mov_b64 exec, s[34:35]
	v_add_u32_e32 v6, 0xa0, v3
	v_cmp_gt_i32_e32 vcc, s25, v6
	s_and_saveexec_b64 s[34:35], vcc
	v_add_u32_e32 v6, s0, v6
	v_ashrrev_i32_e32 v7, 31, v6
	v_lshl_add_u64 v[6:7], v[6:7], 2, s[18:19]
	global_load_dword v8, v[6:7], off
	s_mov_b64 exec, s[34:35]
	v_add_u32_e32 v6, 0xb0, v3
	v_cmp_gt_i32_e32 vcc, s25, v6
	s_and_saveexec_b64 s[34:35], vcc
	v_add_u32_e32 v6, s0, v6
	v_ashrrev_i32_e32 v7, 31, v6
	v_lshl_add_u64 v[6:7], v[6:7], 2, s[18:19]
	global_load_dword v4, v[6:7], off
	s_mov_b64 exec, s[34:35]
	s_waitcnt vmcnt(0)
	v_mul_f32_e32 v20, 0x38800000, v20
	v_mul_f32_e32 v18, 0x38800000, v18
	v_mul_f32_e32 v16, 0x38800000, v16
	v_mul_f32_e32 v14, 0x38800000, v14
	v_mul_f32_e32 v12, 0x38800000, v12
	v_mul_f32_e32 v10, 0x38800000, v10
	v_mul_f32_e32 v8, 0x38800000, v8
	v_mul_f32_e32 v4, 0x38800000, v4
